# cache-policy lever continued: nt hint also on the once-read MoE output (Y) row loads of the combine+norm1 pass
# baseline (speedup 1.0000x reference)
; __device__ __forceinline__ void norm1_phase(Frame& F, KArgs a, int L) {
;     ...
;                 while (mask) {
;                     int pq[4]; float gq[4]; const int nq = __builtin_popcount(mask);
; #pragma unroll
;                     for (int q = 0; q < 4; ++q) {
;                         if (mask) { const int e = __builtin_ctz(mask); mask &= mask - 1u; pq[q] = __builtin_amdgcn_readlane(sl[k], e); gq[q] = __uint_as_float(__builtin_amdgcn_readlane(__float_as_uint(af[k]), e)); }
;                         else { pq[q] = pq[0]; gq[q] = 0.f; }
;                     }
;                     u32x2 y[4][4];
; #pragma unroll
;                     for (int q = 0; q < 4; ++q)
;                         if (q < nq) {
; #pragma unroll
;                             for (int j = 0; j < 4; ++j) y[q][j] = *(const u32x2*)(Y + (size_t)pq[q] * DM + 256 * j + 4 * lane); }
.LBB0_203:
	s_ashr_i32 s77, s76, 31
	s_lshl_b64 s[42:43], s[76:77], 11
	v_lshl_add_u64 v[82:83], v[40:41], 0, s[42:43]
	global_load_dwordx2 v[88:89], v[82:83], off nt
	global_load_dwordx2 v[86:87], v[82:83], off offset:512 nt
	global_load_dwordx2 v[84:85], v[82:83], off offset:1024 nt
	s_nop 0
	global_load_dwordx2 v[82:83], v[82:83], off offset:1536 nt
	s_bcnt1_i32_b32 s24, s24
	s_cmp_gt_u32 s24, 1
	s_cselect_b64 s[76:77], -1, 0
	s_cmp_lt_u32 s24, 2
	s_cbranch_scc0 .LBB0_211
	s_cmp_gt_u32 s24, 2
	s_cselect_b64 s[48:49], -1, 0
	s_cmp_lt_u32 s24, 3
	s_cbranch_scc0 .LBB0_212

; __device__ __forceinline__ void norm1_phase(Frame& F, KArgs a, int L) {
;     ...
;                     for (int q = 0; q < 4; ++q)
;                         if (q < nq) {
; #pragma unroll
;                             for (int j = 0; j < 4; ++j) y[q][j] = *(const u32x2*)(Y + (size_t)pq[q] * DM + 256 * j + 4 * lane); }
.LBB0_206:
	s_ashr_i32 s81, s80, 31
	s_lshl_b64 s[24:25], s[80:81], 11
	v_lshl_add_u64 v[52:53], v[40:41], 0, s[24:25]
	global_load_dwordx2 v[46:47], v[52:53], off nt
	global_load_dwordx2 v[48:49], v[52:53], off offset:512 nt
	global_load_dwordx2 v[50:51], v[52:53], off offset:1024 nt
	s_nop 0
	global_load_dwordx2 v[52:53], v[52:53], off offset:1536 nt

; __device__ __forceinline__ void norm1_phase(Frame& F, KArgs a, int L) {
;     ...
;                     for (int q = 0; q < 4; ++q)
;                         if (q < nq) {
; #pragma unroll
;                             for (int j = 0; j < 4; ++j) y[q][j] = *(const u32x2*)(Y + (size_t)pq[q] * DM + 256 * j + 4 * lane); }
.LBB0_211:
	s_ashr_i32 s49, s48, 31
	s_lshl_b64 s[42:43], s[48:49], 11
	v_lshl_add_u64 v[68:69], v[40:41], 0, s[42:43]
	global_load_dwordx2 v[62:63], v[68:69], off nt
	global_load_dwordx2 v[64:65], v[68:69], off offset:512 nt
	global_load_dwordx2 v[66:67], v[68:69], off offset:1024 nt
	s_nop 0
	global_load_dwordx2 v[68:69], v[68:69], off offset:1536 nt
	s_cmp_gt_u32 s24, 2
	s_cselect_b64 s[48:49], -1, 0
	s_cmp_lt_u32 s24, 3
	s_cbranch_scc1 .LBB0_205
.LBB0_212:
	s_ashr_i32 s31, s30, 31
	s_lshl_b64 s[30:31], s[30:31], 11
	v_lshl_add_u64 v[60:61], v[40:41], 0, s[30:31]
	global_load_dwordx2 v[54:55], v[60:61], off nt
	global_load_dwordx2 v[56:57], v[60:61], off offset:512 nt
	global_load_dwordx2 v[58:59], v[60:61], off offset:1024 nt
	s_nop 0
	global_load_dwordx2 v[60:61], v[60:61], off offset:1536 nt
	s_cmp_gt_u32 s24, 3
	s_cselect_b64 s[30:31], -1, 0
	s_cmp_lt_u32 s24, 4
	s_cbranch_scc0 .LBB0_206
	s_branch .LBB0_207

; __device__ __forceinline__ void norm1_phase(Frame& F, KArgs a, int L) {
;     ...
;                 while (mask) {
;                     int pq[4]; float gq[4]; const int nq = __builtin_popcount(mask);
; #pragma unroll
;                     for (int q = 0; q < 4; ++q) {
;                         if (mask) { const int e = __builtin_ctz(mask); mask &= mask - 1u; pq[q] = __builtin_amdgcn_readlane(sl[k], e); gq[q] = __uint_as_float(__builtin_amdgcn_readlane(__float_as_uint(af[k]), e)); }
;                         else { pq[q] = pq[0]; gq[q] = 0.f; }
;                     }
;                     u32x2 y[4][4];
; #pragma unroll
;                     for (int q = 0; q < 4; ++q)
;                         if (q < nq) {
; #pragma unroll
;                             for (int j = 0; j < 4; ++j) y[q][j] = *(const u32x2*)(Y + (size_t)pq[q] * DM + 256 * j + 4 * lane); }
.LBB0_229:
	s_ashr_i32 s49, s48, 31
	s_lshl_b64 s[24:25], s[48:49], 11
	v_lshl_add_u64 v[34:35], v[40:41], 0, s[24:25]
	global_load_dwordx2 v[72:73], v[34:35], off nt
	global_load_dwordx2 v[70:71], v[34:35], off offset:512 nt
	global_load_dwordx2 v[36:37], v[34:35], off offset:1024 nt
	s_nop 0
	global_load_dwordx2 v[34:35], v[34:35], off offset:1536 nt
	s_bcnt1_i32_b32 s11, s11
	s_cmp_gt_u32 s11, 1
	s_cselect_b64 s[48:49], -1, 0
	s_cmp_lt_u32 s11, 2
	s_cbranch_scc0 .LBB0_237
	s_cmp_gt_u32 s11, 2
	s_cselect_b64 s[40:41], -1, 0
	s_cmp_lt_u32 s11, 3
	s_cbranch_scc0 .LBB0_238

; __device__ __forceinline__ void norm1_phase(Frame& F, KArgs a, int L) {
;     ...
;                     for (int q = 0; q < 4; ++q)
;                         if (q < nq) {
; #pragma unroll
;                             for (int j = 0; j < 4; ++j) y[q][j] = *(const u32x2*)(Y + (size_t)pq[q] * DM + 256 * j + 4 * lane); }
.LBB0_232:
	s_ashr_i32 s51, s50, 31
	s_lshl_b64 s[24:25], s[50:51], 11
	v_lshl_add_u64 v[52:53], v[40:41], 0, s[24:25]
	global_load_dwordx2 v[46:47], v[52:53], off nt
	global_load_dwordx2 v[48:49], v[52:53], off offset:512 nt
	global_load_dwordx2 v[50:51], v[52:53], off offset:1024 nt
	s_nop 0
	global_load_dwordx2 v[52:53], v[52:53], off offset:1536 nt

; __device__ __forceinline__ void norm1_phase(Frame& F, KArgs a, int L) {
;     ...
;                     for (int q = 0; q < 4; ++q)
;                         if (q < nq) {
; #pragma unroll
;                             for (int j = 0; j < 4; ++j) y[q][j] = *(const u32x2*)(Y + (size_t)pq[q] * DM + 256 * j + 4 * lane); }
.LBB0_237:
	s_ashr_i32 s41, s40, 31
	s_lshl_b64 s[24:25], s[40:41], 11
	v_lshl_add_u64 v[68:69], v[40:41], 0, s[24:25]
	global_load_dwordx2 v[62:63], v[68:69], off nt
	global_load_dwordx2 v[64:65], v[68:69], off offset:512 nt
	global_load_dwordx2 v[66:67], v[68:69], off offset:1024 nt
	s_nop 0
	global_load_dwordx2 v[68:69], v[68:69], off offset:1536 nt
	s_cmp_gt_u32 s11, 2
	s_cselect_b64 s[40:41], -1, 0
	s_cmp_lt_u32 s11, 3
	s_cbranch_scc1 .LBB0_231
.LBB0_238:
	s_ashr_i32 s31, s30, 31
	s_lshl_b64 s[24:25], s[30:31], 11
	v_lshl_add_u64 v[60:61], v[40:41], 0, s[24:25]
	global_load_dwordx2 v[54:55], v[60:61], off nt
	global_load_dwordx2 v[56:57], v[60:61], off offset:512 nt
	global_load_dwordx2 v[58:59], v[60:61], off offset:1024 nt
	s_nop 0
	global_load_dwordx2 v[60:61], v[60:61], off offset:1536 nt
	s_cmp_gt_u32 s11, 3
	s_cselect_b64 s[30:31], -1, 0
	s_cmp_lt_u32 s11, 4
	s_cbranch_scc0 .LBB0_232
	s_branch .LBB0_233
